# v123 + NORM0 forget-gate scan: rank-16 f32 dot moved from v_pk_fma_f32 to f32-operand v_mfma_f32_4x4x1_16b_f32 (same fma order), 4 tokens per iteration
# baseline (speedup 1.0000x reference)
; __device__ __forceinline__ void p0_norm_gl(Frame& F) {
;     ...
;         if (F.tid < 64) { float t = 0.f;
; #pragma unroll
;             for (int w = 0; w < 8; ++w) t += sqp[w * 64 + F.tid];
;             const float rstd = 1.0f / sqrtf(t * (1.0f / D) + EPS); rs[F.tid] = rstd; RSTD[ch * CHK + F.tid] = rstd; }
;         __syncthreads();
; #pragma unroll
;         for (int i = 0; i < 2; ++i) { const int idx = F.tid + 512 * i; float t = 0.f;
; #pragma unroll
;             for (int w = 0; w < 8; ++w) t += part[w * 1024 + idx];
;             glc[idx] = t * rs[idx >> 4]; }
;         __syncthreads();
;         {
;             typedef float v2f __attribute__((ext_vector_type(2)));
;             const int c0 = F.tid, c1 = F.tid + 512; v2f wv[16];
; #pragma unroll
;             for (int r = 0; r < 16; ++r) wv[r] = (v2f){w2[r * KD + c0], w2[r * KD + c1]};
;             const v2f bv = (v2f){bgk[c0], bgk[c1]}; float cuma = 0.f, cumb = 0.f;
.LBB0_180:
	s_or_b64 exec, exec, s[12:13]
	s_waitcnt lgkmcnt(0)
	s_barrier
	ds_read2st64_b32 v[2:3], v139 offset1:8
	ds_read2st64_b32 v[4:5], v139 offset0:16 offset1:24
	ds_read2st64_b32 v[6:7], v139 offset0:32 offset1:40
	ds_read2st64_b32 v[8:9], v139 offset0:48 offset1:56
	ds_read2st64_b32 v[10:11], v139 offset0:64 offset1:72
	s_waitcnt lgkmcnt(4)
	v_add_f32_e32 v2, 0, v2
	v_add_f32_e32 v3, 0, v3
	s_waitcnt lgkmcnt(3)
	v_add_f32_e32 v2, v2, v4
	v_add_f32_e32 v3, v3, v5
	s_waitcnt lgkmcnt(2)
	v_add_f32_e32 v2, v2, v6
	ds_read2st64_b32 v[12:13], v139 offset0:80 offset1:88
	ds_read2st64_b32 v[14:15], v139 offset0:96 offset1:104
	ds_read2st64_b32 v[16:17], v139 offset0:112 offset1:120
	v_add_f32_e32 v3, v3, v7
	s_waitcnt lgkmcnt(4)
	v_add_f32_e32 v2, v2, v8
	ds_read_b32 v4, v150 offset:38912
	ds_read_b32 v6, v151 offset:38912
	v_add_f32_e32 v3, v3, v9
	s_waitcnt lgkmcnt(5)
	v_add_f32_e32 v2, v2, v10
	v_add_f32_e32 v3, v3, v11
	s_waitcnt lgkmcnt(4)
	v_add_f32_e32 v2, v2, v12
	v_add_f32_e32 v3, v3, v13
	s_waitcnt lgkmcnt(3)
	v_add_f32_e32 v2, v2, v14
	v_add_f32_e32 v3, v3, v15
	s_waitcnt lgkmcnt(2)
	v_add_f32_e32 v2, v2, v16
	v_add_f32_e32 v3, v3, v17
	s_waitcnt lgkmcnt(1)
	v_mul_f32_e32 v2, v2, v4
	s_waitcnt lgkmcnt(0)
	v_mul_f32_e32 v3, v3, v6
	ds_write2st64_b32 v139, v2, v3 offset0:136 offset1:144
	s_waitcnt lgkmcnt(0)
	s_barrier
	global_load_dword v2, v[72:73], off
	global_load_dword v3, v[72:73], off offset:2048
	global_load_dword v4, v[74:75], off
	global_load_dword v5, v[76:77], off
	global_load_dword v6, v[78:79], off
	global_load_dword v7, v[80:81], off
	global_load_dword v8, v[82:83], off
	global_load_dword v9, v[84:85], off
	global_load_dword v10, v[86:87], off
	global_load_dword v11, v[88:89], off
	global_load_dword v12, v[90:91], off
	global_load_dword v13, v[92:93], off
	global_load_dword v14, v[94:95], off
	global_load_dword v15, v[96:97], off
	global_load_dword v16, v[98:99], off
	global_load_dword v17, v[100:101], off
	global_load_dword v18, v[102:103], off
	global_load_dword v19, v[104:105], off
	global_load_dword v20, v[106:107], off
	global_load_dword v21, v[108:109], off
	global_load_dword v22, v[110:111], off
	global_load_dword v23, v[112:113], off
	global_load_dword v24, v[114:115], off
	global_load_dword v25, v[116:117], off
	global_load_dword v26, v[118:119], off
	global_load_dword v27, v[120:121], off
	global_load_dword v28, v[122:123], off
	global_load_dword v29, v[124:125], off
	global_load_dword v30, v[126:127], off
	global_load_dword v31, v[128:129], off
	global_load_dword v32, v[130:131], off
	global_load_dword v33, v[132:133], off
	global_load_dword v34, v[134:135], off
	global_load_dword v35, v[134:135], off offset:2048
	v_mov_b32_e32 v36, 0
	s_mov_b32 s45, 0
	s_mov_b32 s46, s3
	v_mov_b32_e32 v37, v36
	s_waitcnt vmcnt(0)
	v_and_b32_e32 v182, 3, v0
	v_lshlrev_b32_e32 v182, 6, v182
	v_mov_b32_e32 v184, v34
	v_mov_b32_e32 v185, v34
	v_mov_b32_e32 v186, v34
	v_mov_b32_e32 v187, v34
	v_mov_b32_e32 v188, v35
	v_mov_b32_e32 v189, v35
	v_mov_b32_e32 v190, v35
	v_mov_b32_e32 v191, v35
; __device__ __forceinline__ void p0_norm_gl(Frame& F) {
;     ...
;             for (int t = 0; t < CHK; ++t) {
;                 v2f z = bv;
; #pragma unroll
;                 for (int r = 0; r < 16; ++r) { const float g = glc[t * 16 + r]; z = __builtin_elementwise_fma(wv[r], (v2f){g, g}, z); }
;                 const float za = z.x, zb = z.y;
;                 const float la = fminf(za, 0.f) - __logf(1.0f + __expf(-fabsf(za))), lb = fminf(zb, 0.f) - __logf(1.0f + __expf(-fabsf(zb)));
;                 cuma += la * (1.0f / 16.0f); cumb += lb * (1.0f / 16.0f);
;                 BC[(size_t)(ch * CHK + t) * KD + c0] = cuma; BC[(size_t)(ch * CHK + t) * KD + c1] = cumb;
;             }
.LBB0_181:
	v_add_u32_e32 v144, s45, v182
	ds_read_b128 v[38:41], v144 offset:34816
	ds_read_b128 v[42:45], v144 offset:34832
	ds_read_b128 v[46:49], v144 offset:34848
	ds_read_b128 v[50:53], v144 offset:34864
	s_waitcnt lgkmcnt(3)
	v_mfma_f32_4x4x1_16b_f32 v[192:195], v38, v2, v[184:187]
	v_mfma_f32_4x4x1_16b_f32 v[196:199], v38, v3, v[188:191]
	s_nop 0
	v_mfma_f32_4x4x1_16b_f32 v[192:195], v39, v4, v[192:195]
	v_mfma_f32_4x4x1_16b_f32 v[196:199], v39, v5, v[196:199]
	s_nop 0
	v_mfma_f32_4x4x1_16b_f32 v[192:195], v40, v6, v[192:195]
	v_mfma_f32_4x4x1_16b_f32 v[196:199], v40, v7, v[196:199]
	s_nop 0
	v_mfma_f32_4x4x1_16b_f32 v[192:195], v41, v8, v[192:195]
	v_mfma_f32_4x4x1_16b_f32 v[196:199], v41, v9, v[196:199]
	s_nop 0
	s_waitcnt lgkmcnt(2)
	v_mfma_f32_4x4x1_16b_f32 v[192:195], v42, v10, v[192:195]
	v_mfma_f32_4x4x1_16b_f32 v[196:199], v42, v11, v[196:199]
	s_nop 0
	v_mfma_f32_4x4x1_16b_f32 v[192:195], v43, v12, v[192:195]
	v_mfma_f32_4x4x1_16b_f32 v[196:199], v43, v13, v[196:199]
	s_nop 0
	v_mfma_f32_4x4x1_16b_f32 v[192:195], v44, v14, v[192:195]
	v_mfma_f32_4x4x1_16b_f32 v[196:199], v44, v15, v[196:199]
	s_nop 0
	v_mfma_f32_4x4x1_16b_f32 v[192:195], v45, v16, v[192:195]
	v_mfma_f32_4x4x1_16b_f32 v[196:199], v45, v17, v[196:199]
	s_nop 0
	s_waitcnt lgkmcnt(1)
	v_mfma_f32_4x4x1_16b_f32 v[192:195], v46, v18, v[192:195]
	v_mfma_f32_4x4x1_16b_f32 v[196:199], v46, v19, v[196:199]
	s_nop 0
	v_mfma_f32_4x4x1_16b_f32 v[192:195], v47, v20, v[192:195]
	v_mfma_f32_4x4x1_16b_f32 v[196:199], v47, v21, v[196:199]
	s_nop 0
	v_mfma_f32_4x4x1_16b_f32 v[192:195], v48, v22, v[192:195]
	v_mfma_f32_4x4x1_16b_f32 v[196:199], v48, v23, v[196:199]
	s_nop 0
	v_mfma_f32_4x4x1_16b_f32 v[192:195], v49, v24, v[192:195]
	v_mfma_f32_4x4x1_16b_f32 v[196:199], v49, v25, v[196:199]
	s_nop 0
	s_waitcnt lgkmcnt(0)
	v_mfma_f32_4x4x1_16b_f32 v[192:195], v50, v26, v[192:195]
	v_mfma_f32_4x4x1_16b_f32 v[196:199], v50, v27, v[196:199]
	s_nop 0
	v_mfma_f32_4x4x1_16b_f32 v[192:195], v51, v28, v[192:195]
	v_mfma_f32_4x4x1_16b_f32 v[196:199], v51, v29, v[196:199]
	s_nop 0
	v_mfma_f32_4x4x1_16b_f32 v[192:195], v52, v30, v[192:195]
	v_mfma_f32_4x4x1_16b_f32 v[196:199], v52, v31, v[196:199]
	s_nop 0
	v_mfma_f32_4x4x1_16b_f32 v[192:195], v53, v32, v[192:195]
	v_mfma_f32_4x4x1_16b_f32 v[196:199], v53, v33, v[196:199]
	s_nop 5
	v_mul_f32_e64 v44, |v192|, s59
	v_mul_f32_e64 v45, |v196|, s59
	v_min_f32_e32 v43, 0, v192
	v_min_f32_e32 v42, 0, v196
	v_min_f32_e32 v39, 0, v193
	v_mul_f32_e64 v40, |v193|, s59
	v_min_f32_e32 v38, 0, v197
	v_mul_f32_e64 v41, |v197|, s59
	v_exp_f32_e32 v44, v44
	v_exp_f32_e32 v45, v45
	v_exp_f32_e32 v40, v40
	v_exp_f32_e32 v41, v41
	s_add_i32 s10, s46, 1
	s_ashr_i32 s11, s10, 31
	s_ashr_i32 s47, s46, 31
	s_lshl_b64 s[10:11], s[10:11], 12
	v_add_f32_e32 v44, 1.0, v44
	v_add_f32_e32 v45, 1.0, v45
	s_lshl_b64 s[12:13], s[46:47], 12
	v_lshl_add_u64 v[160:161], v[136:137], 0, s[10:11]
	v_add_f32_e32 v40, 1.0, v40
	v_add_f32_e32 v41, 1.0, v41
	v_lshl_add_u64 v[148:149], v[136:137], 0, s[12:13]
	v_log_f32_e32 v44, v44
	v_log_f32_e32 v45, v45
	v_log_f32_e32 v40, v40
	v_log_f32_e32 v41, v41
	v_mul_f32_e32 v50, 0x3f317217, v44
	v_mul_f32_e32 v51, 0x3f317217, v45
	v_mul_f32_e32 v52, 0x3f317217, v40
	v_mul_f32_e32 v53, 0x3f317217, v41
	v_fma_f32 v50, v44, s61, -v50
	v_fma_f32 v51, v45, s61, -v51
	v_fma_f32 v52, v40, s61, -v52
	v_fma_f32 v53, v41, s61, -v53
	v_fmac_f32_e32 v50, 0x3377d1cf, v44
	v_fmac_f32_e32 v51, 0x3377d1cf, v45
	v_fmac_f32_e32 v52, 0x3377d1cf, v40
	v_fmac_f32_e32 v53, 0x3377d1cf, v41
	v_fmac_f32_e32 v50, 0x3f317217, v44
	v_fmac_f32_e32 v51, 0x3f317217, v45
	v_fmac_f32_e32 v52, 0x3f317217, v40
	v_fmac_f32_e32 v53, 0x3f317217, v41
	v_pk_add_f32 v[40:41], v[42:43], v[50:51] op_sel:[0,1] op_sel_hi:[1,0] neg_lo:[0,1] neg_hi:[0,1]
	s_addk_i32 s45, 0x80
	s_add_i32 s46, s46, 2
	v_pk_add_f32 v[38:39], v[38:39], v[52:53] op_sel:[0,1] op_sel_hi:[1,0] neg_lo:[0,1] neg_hi:[0,1]
	v_pk_fma_f32 v[36:37], v[40:41], s[42:43], v[36:37] op_sel_hi:[1,0,1]
	s_cmpk_lg_i32 s45, 0x1000
	global_store_dword v[148:149], v37, off
	global_store_dword v[148:149], v36, off offset:2048
	v_pk_fma_f32 v[36:37], v[38:39], s[42:43], v[36:37] op_sel_hi:[1,0,1]
	global_store_dword v[160:161], v37, off
	global_store_dword v[160:161], v36, off offset:2048
	v_mul_f32_e64 v44, |v194|, s59
	v_mul_f32_e64 v45, |v198|, s59
	v_min_f32_e32 v43, 0, v194
	v_min_f32_e32 v42, 0, v198
	v_min_f32_e32 v39, 0, v195
	v_mul_f32_e64 v40, |v195|, s59
	v_min_f32_e32 v38, 0, v199
	v_mul_f32_e64 v41, |v199|, s59
	v_exp_f32_e32 v44, v44
	v_exp_f32_e32 v45, v45
	v_exp_f32_e32 v40, v40
	v_exp_f32_e32 v41, v41
	s_add_i32 s10, s46, 1
	s_ashr_i32 s11, s10, 31
	s_ashr_i32 s47, s46, 31
	s_lshl_b64 s[10:11], s[10:11], 12
	v_add_f32_e32 v44, 1.0, v44
	v_add_f32_e32 v45, 1.0, v45
	s_lshl_b64 s[12:13], s[46:47], 12
	v_lshl_add_u64 v[160:161], v[136:137], 0, s[10:11]
	v_add_f32_e32 v40, 1.0, v40
	v_add_f32_e32 v41, 1.0, v41
	v_lshl_add_u64 v[148:149], v[136:137], 0, s[12:13]
	v_log_f32_e32 v44, v44
	v_log_f32_e32 v45, v45
	v_log_f32_e32 v40, v40
	v_log_f32_e32 v41, v41
	v_mul_f32_e32 v50, 0x3f317217, v44
	v_mul_f32_e32 v51, 0x3f317217, v45
	v_mul_f32_e32 v52, 0x3f317217, v40
	v_mul_f32_e32 v53, 0x3f317217, v41
	v_fma_f32 v50, v44, s61, -v50
	v_fma_f32 v51, v45, s61, -v51
	v_fma_f32 v52, v40, s61, -v52
	v_fma_f32 v53, v41, s61, -v53
	v_fmac_f32_e32 v50, 0x3377d1cf, v44
	v_fmac_f32_e32 v51, 0x3377d1cf, v45
	v_fmac_f32_e32 v52, 0x3377d1cf, v40
	v_fmac_f32_e32 v53, 0x3377d1cf, v41
	v_fmac_f32_e32 v50, 0x3f317217, v44
	v_fmac_f32_e32 v51, 0x3f317217, v45
	v_fmac_f32_e32 v52, 0x3f317217, v40
	v_fmac_f32_e32 v53, 0x3f317217, v41
	v_pk_add_f32 v[40:41], v[42:43], v[50:51] op_sel:[0,1] op_sel_hi:[1,0] neg_lo:[0,1] neg_hi:[0,1]
	s_addk_i32 s45, 0x80
	s_add_i32 s46, s46, 2
	v_pk_add_f32 v[38:39], v[38:39], v[52:53] op_sel:[0,1] op_sel_hi:[1,0] neg_lo:[0,1] neg_hi:[0,1]
	v_pk_fma_f32 v[36:37], v[40:41], s[42:43], v[36:37] op_sel_hi:[1,0,1]
	s_cmpk_lg_i32 s45, 0x1000
	global_store_dword v[148:149], v37, off
	global_store_dword v[148:149], v36, off offset:2048
	v_pk_fma_f32 v[36:37], v[38:39], s[42:43], v[36:37] op_sel_hi:[1,0,1]
	global_store_dword v[160:161], v37, off
	global_store_dword v[160:161], v36, off offset:2048
	s_cbranch_scc1 .LBB0_181
	s_add_i32 s44, s44, s34
	s_add_i32 s3, s3, s35
	v_lshl_add_u64 v[140:141], v[140:141], 0, s[24:25]
	s_cmpk_lt_i32 s44, 0x100
	v_lshl_add_u64 v[142:143], v[142:143], 0, s[26:27]
	s_barrier
	s_cbranch_scc1 .LBB0_166
